# edge1: counted gather waits, consumer of gather k waits vmcnt(31-k) instead of one vmcnt(0) for all 32 rows
# baseline (speedup 1.0000x reference)
.LBB4_10:
	s_and_b64 s[2:3], exec, s[2:3]
	s_or_b64 s[14:15], s[2:3], s[14:15]
	v_readlane_b32 s2, v50, 31
	s_bfe_u32 s3, s2, 0x80008
	v_lshl_or_b32 v0, s3, 7, v73
	ds_read_u16 v0, v0
	s_bfe_u32 s2, s2, 0x100010
	s_lshl_b32 s10, s2, 8
	s_waitcnt vmcnt(0)
	v_fma_mix_f32 v32, v15, v81, v32 op_sel:[0,1,0] op_sel_hi:[0,1,0]
	v_fma_mix_f32 v33, v15, v81, v33 op_sel_hi:[0,1,0]
	s_nop 0
	v_cndmask_b32_sdwa v95, v51, v68, vcc dst_sel:DWORD dst_unused:UNUSED_PAD src0_sel:WORD_1 src1_sel:DWORD
	s_waitcnt lgkmcnt(0)
	v_fma_mix_f32 v2, v0, v33, v32 op_sel_hi:[1,0,0]
	s_add_u32 s58, s60, s10
	s_addc_u32 s59, s61, 0
	s_cmp_lg_u64 s[20:21], 0
	s_cselect_b32 s58, s58, s62
	s_cselect_b32 s59, s59, s63
	s_nop 0
	s_nop 0
	s_add_u32 s62, s62, 0x100000
	s_addc_u32 s63, s63, 0
	v_mov_b64_e32 v[48:49], v[56:57]
	v_mov_b64_e32 v[50:51], v[58:59]
	global_store_dword v79, v2, s[58:59] sc1
	s_andn2_b64 exec, exec, s[14:15]
	s_cbranch_execz .LBB4_73

.Lprio_e1_done:
	s_mov_b32 s93, s94
	s_add_u32 s94, s94, 0x1000
	s_cmp_lt_u32 s94, 0x61a8
	s_cselect_b32 s95, s94, s93
	s_lshl_b32 s95, s95, 9
	s_add_u32 s56, s8, s95
	s_addc_u32 s57, s9, 0
	ds_bpermute_b32 v126, v125, v51
	v_sub_f32_e32 v39, v48, v67
	v_fmamk_f32 v32, v39, 0x4297576a, v65
	v_fmamk_f32 v33, v39, 0x4297576a, v76
	v_med3_f32 v35, v32, s22, v74
	v_med3_f32 v37, v33, s22, v74
	v_mul_f32_e64 v32, v35, -v35
	v_fmamk_f32 v34, v35, 0x4019be61, v75
	v_mul_f32_e64 v33, v37, -v37
	v_fmamk_f32 v35, v35, 0xc019be61, v75
	v_exp_f32_e32 v32, v32
	v_exp_f32_e32 v33, v33
	v_exp_f32_e32 v36, v35
	v_fmamk_f32 v35, v37, 0x4019be61, v75
	v_exp_f32_e32 v34, v34
	v_exp_f32_e32 v35, v35
	v_fmamk_f32 v37, v37, 0xc019be61, v75
	v_exp_f32_e32 v37, v37
	v_pk_mul_f32 v[32:33], v[48:49], v[32:33] op_sel:[1,0]
	ds_read_b128 v[28:31], v69
	ds_read_b128 v[24:27], v69 offset:1024
	ds_read_b128 v[20:23], v69 offset:2048
	ds_read_b128 v[16:19], v69 offset:3072
	ds_read_b128 v[0:3], v70
	ds_read_b128 v[4:7], v70 offset:32
	ds_read_b128 v[8:11], v70 offset:64
	ds_read_b128 v[12:15], v70 offset:96
	v_pk_mul_f32 v[44:45], v[34:35], v[32:33]
	v_pk_mul_f32 v[34:35], v[34:35], s[16:17] op_sel_hi:[1,0]
	v_mov_b32_e32 v99, v80
	v_fmamk_f32 v38, v39, 0x4297576a, v77
	v_fmamk_f32 v39, v39, 0x4297576a, v78
	v_pk_mul_f32 v[46:47], v[34:35], v[44:45]
	v_pk_mul_f32 v[34:35], v[34:35], s[16:17] op_sel_hi:[1,0]
	v_pk_mul_f32 v[80:81], v[36:37], v[32:33]
	v_pk_mul_f32 v[36:37], v[36:37], s[16:17] op_sel_hi:[1,0]
	v_med3_f32 v41, v38, s22, v74
	v_med3_f32 v43, v39, s22, v74
	v_pk_mul_f32 v[58:59], v[34:35], v[46:47]
	v_pk_mul_f32 v[34:35], v[34:35], s[16:17] op_sel_hi:[1,0]
	v_pk_mul_f32 v[82:83], v[36:37], v[80:81]
	v_pk_mul_f32 v[36:37], v[36:37], s[16:17] op_sel_hi:[1,0]
	v_mul_f32_e64 v38, v41, -v41
	v_fmamk_f32 v40, v41, 0x4019be61, v75
	v_mul_f32_e64 v39, v43, -v43
	v_fmamk_f32 v41, v41, 0xc019be61, v75
	v_pk_mul_f32 v[34:35], v[34:35], v[58:59]
	v_pk_mul_f32 v[36:37], v[36:37], v[82:83]
	v_exp_f32_e32 v38, v38
	v_exp_f32_e32 v39, v39
	v_exp_f32_e32 v42, v41
	v_fmamk_f32 v41, v43, 0x4019be61, v75
	v_cvt_pk_f16_f32 v56, v44, v46
	v_cvt_pk_f16_f32 v54, v36, v82
	v_cvt_pk_f16_f32 v57, v58, v34
	v_cvt_pk_f16_f32 v55, v80, v32
	v_exp_f32_e32 v40, v40
	v_exp_f32_e32 v41, v41
	s_waitcnt lgkmcnt(0)
	v_mfma_f32_32x32x16_f16 v[0:15], v[28:31], v[54:57], v[0:15]
	v_mul_f32_e64 v38, v49, v38
	v_mul_f32_e64 v39, v49, v39
	v_fmamk_f32 v43, v43, 0xc019be61, v75
	v_mul_f32_e64 v84, v40, v38
	v_mul_f32_e64 v85, v41, v39
	v_pk_mul_f32 v[40:41], v[40:41], s[16:17] op_sel_hi:[1,0]
	v_cvt_pk_f16_f32 v30, v45, v47
	v_pk_mul_f32 v[86:87], v[40:41], v[84:85]
	v_pk_mul_f32 v[28:29], v[40:41], s[16:17] op_sel_hi:[1,0]
	v_cvt_pk_f16_f32 v31, v59, v35
	v_pk_mul_f32 v[40:41], v[28:29], v[86:87]
	v_pk_mul_f32 v[28:29], v[28:29], s[16:17] op_sel_hi:[1,0]
	v_exp_f32_e32 v43, v43
	v_pk_mul_f32 v[88:89], v[28:29], v[40:41]
	v_cvt_pk_f16_f32 v28, v37, v83
	v_cvt_pk_f16_f32 v29, v81, v33
	v_pk_mul_f32 v[36:37], v[42:43], v[38:39]
	v_pk_mul_f32 v[42:43], v[42:43], s[16:17] op_sel_hi:[1,0]
	v_mfma_f32_32x32x16_f16 v[0:15], v[24:27], v[28:31], v[0:15]
	v_mul_f32_e64 v32, v42, v36
	v_mul_f32_e64 v33, v43, v37
	v_mul_f32_e64 v24, v42, s16
	v_mul_f32_e64 v25, v43, s16
	v_cvt_pk_f16_f32 v26, v84, v86
	v_pk_mul_f32 v[34:35], v[24:25], v[32:33]
	v_cvt_pk_f16_f32 v27, v40, v88
	v_cvt_pk_f16_f32 v24, v34, v32
	v_cvt_pk_f16_f32 v25, v36, v38
	v_cvt_pk_f16_f32 v84, v85, v87
	v_cvt_pk_f16_f32 v82, v35, v33
	v_mfma_f32_32x32x16_f16 v[0:15], v[20:23], v[24:27], v[0:15]
	ds_read_b128 v[20:23], v69 offset:4096
	v_cvt_pk_f16_f32 v85, v41, v89
	v_cvt_pk_f16_f32 v83, v37, v39
	ds_read_b128 v[32:35], v70 offset:128
	ds_read_b128 v[36:39], v70 offset:160
	ds_read_b128 v[40:43], v70 offset:192
	ds_read_b128 v[44:47], v70 offset:224
	s_nop 0
	v_add_u32_e32 v64, s12, v64
	v_perm_b32 v127, v126, v51, s64
	s_nop 0
	v_readlane_b32 s70, v127, 0
	v_readlane_b32 s71, v127, 1
	v_readlane_b32 s72, v127, 2
	v_readlane_b32 s73, v127, 3
	v_readlane_b32 s74, v127, 4
	v_readlane_b32 s75, v127, 5
	v_readlane_b32 s76, v127, 6
	v_readlane_b32 s77, v127, 7
	v_readlane_b32 s78, v127, 8
	v_readlane_b32 s79, v127, 9
	v_readlane_b32 s80, v127, 10
	v_readlane_b32 s81, v127, 11
	v_readlane_b32 s82, v127, 12
	v_readlane_b32 s83, v127, 13
	v_readlane_b32 s84, v127, 14
	v_readlane_b32 s85, v127, 15
	s_pack_ll_b32_b16 s48, s70, 0
	v_mfma_f32_32x32x16_f16 v[0:15], v[16:19], v[82:85], v[0:15]
	ds_read_b128 v[16:19], v69 offset:5120
	s_nop 0
	s_lshl_b32 s48, s48, 8
	s_and_b32 s48, s48, 0xffff00
	s_pack_ll_b32_b16 s47, s71, 0
	s_add_u32 s48, s4, s48
	s_addc_u32 s49, s5, 0
	s_waitcnt lgkmcnt(1)
	v_mfma_f32_32x32x16_f16 v[32:47], v[20:23], v[54:57], v[32:47]
	ds_read_b128 v[20:23], v69 offset:6144
	s_lshl_b32 s47, s47, 8
	s_and_b32 s47, s47, 0xffff00
	s_pack_ll_b32_b16 s46, s72, 0
	s_pack_ll_b32_b16 s45, s73, 0
	s_pack_ll_b32_b16 s44, s74, 0
	s_pack_ll_b32_b16 s43, s75, 0
	s_waitcnt lgkmcnt(1)
	v_mfma_f32_32x32x16_f16 v[32:47], v[16:19], v[28:31], v[32:47]
	s_nop 0
	s_nop 0
	s_mov_b64 vcc, 0
	s_nop 0
	s_nop 0
	s_pack_ll_b32_b16 s3, s76, 0
	s_pack_ll_b32_b16 s2, s77, 0
	s_waitcnt lgkmcnt(0)
	v_mfma_f32_32x32x16_f16 v[32:47], v[20:23], v[24:27], v[32:47]
	s_nop 0
	s_nop 0
	s_pack_ll_b32_b16 s36, s78, 0
	s_pack_ll_b32_b16 s35, s79, 0
	s_pack_ll_b32_b16 s34, s80, 0
	s_pack_ll_b32_b16 s33, s81, 0
	s_pack_ll_b32_b16 s31, s82, 0
	s_pack_ll_b32_b16 s30, s83, 0
	s_pack_ll_b32_b16 s29, s84, 0
	s_pack_ll_b32_b16 s28, s85, 0
	s_pack_hh_b32_b16 s27, s70, 0
	s_pack_hh_b32_b16 s26, s71, 0
	s_pack_hh_b32_b16 s25, s72, 0
	s_pack_hh_b32_b16 s24, s73, 0
	s_pack_hh_b32_b16 s23, s74, 0
	s_pack_hh_b32_b16 s42, s75, 0
	s_pack_hh_b32_b16 s41, s76, 0
	s_pack_hh_b32_b16 s40, s77, 0
	s_pack_hh_b32_b16 s39, s78, 0
	s_pack_hh_b32_b16 s38, s79, 0
	s_pack_hh_b32_b16 s37, s80, 0
	s_pack_hh_b32_b16 s21, s81, 0
	s_pack_hh_b32_b16 s20, s82, 0
	s_pack_hh_b32_b16 s19, s83, 0
	s_pack_hh_b32_b16 s18, s84, 0
	s_pack_hh_b32_b16 s10, s85, 0
	ds_read_b128 v[16:19], v69 offset:7168
	s_nop 0
	global_load_dwordx4 v[56:59], v124, s[56:57]
	global_load_dword v80, v124, s[56:57] offset:24
	global_load_dword v51, v124, s[56:57] offset:-8
	global_load_dword v112, v79, s[48:49]
	s_add_u32 s48, s4, s47
	s_addc_u32 s49, s5, 0
	s_lshl_b32 s46, s46, 8
	s_and_b32 s46, s46, 0xffff00
	s_add_u32 s46, s4, s46
	s_addc_u32 s47, s5, 0
	s_lshl_b32 s45, s45, 8
	s_and_b32 s45, s45, 0xffff00
	global_load_dword v110, v79, s[48:49]
	global_load_dword v108, v79, s[46:47]
	s_add_u32 s46, s4, s45
	s_addc_u32 s47, s5, 0
	s_lshl_b32 s44, s44, 8
	s_and_b32 s44, s44, 0xffff00
	s_add_u32 s44, s4, s44
	s_addc_u32 s45, s5, 0
	s_lshl_b32 s43, s43, 8
	s_and_b32 s43, s43, 0xffff00
	global_load_dword v106, v79, s[46:47]
	global_load_dword v104, v79, s[44:45]
	s_add_u32 s44, s4, s43
	s_addc_u32 s45, s5, 0
	s_lshl_b32 s3, s3, 8
	s_and_b32 s3, s3, 0xffff00
	global_load_dword v102, v79, s[44:45]
	s_add_u32 s44, s4, s3
	s_addc_u32 s45, s5, 0
	s_lshl_b32 s2, s2, 8
	s_and_b32 s2, s2, 0xffff00
	s_add_u32 s2, s4, s2
	global_load_dword v100, v79, s[44:45]
	s_addc_u32 s3, s5, 0
	global_load_dword v114, v79, s[2:3]
	s_lshl_b32 s2, s36, 8
	s_and_b32 s2, s2, 0xffff00
	s_add_u32 s2, s4, s2
	s_addc_u32 s3, s5, 0
	global_load_dword v113, v79, s[2:3]
	s_lshl_b32 s2, s35, 8
	s_and_b32 s2, s2, 0xffff00
	s_add_u32 s2, s4, s2
	s_addc_u32 s3, s5, 0
	global_load_dword v111, v79, s[2:3]
	s_lshl_b32 s2, s34, 8
	s_and_b32 s2, s2, 0xffff00
	s_add_u32 s2, s4, s2
	s_addc_u32 s3, s5, 0
	global_load_dword v109, v79, s[2:3]
	s_lshl_b32 s2, s33, 8
	s_and_b32 s2, s2, 0xffff00
	s_add_u32 s2, s4, s2
	s_addc_u32 s3, s5, 0
	global_load_dword v107, v79, s[2:3]
	s_lshl_b32 s2, s31, 8
	s_and_b32 s2, s2, 0xffff00
	s_add_u32 s2, s4, s2
	s_addc_u32 s3, s5, 0
	global_load_dword v105, v79, s[2:3]
	s_lshl_b32 s2, s30, 8
	s_and_b32 s2, s2, 0xffff00
	s_add_u32 s2, s4, s2
	s_addc_u32 s3, s5, 0
	global_load_dword v103, v79, s[2:3]
	s_lshl_b32 s2, s29, 8
	s_and_b32 s2, s2, 0xffff00
	s_add_u32 s2, s4, s2
	s_addc_u32 s3, s5, 0
	global_load_dword v101, v79, s[2:3]
	s_lshl_b32 s2, s28, 8
	s_and_b32 s2, s2, 0xffff00
	s_add_u32 s2, s4, s2
	s_addc_u32 s3, s5, 0
	global_load_dword v98, v79, s[2:3]
	s_lshl_b32 s2, s27, 8
	s_and_b32 s2, s2, 0xffff00
	s_add_u32 s2, s4, s2
	s_addc_u32 s3, s5, 0
	global_load_dword v97, v79, s[2:3]
	s_lshl_b32 s2, s26, 8
	s_and_b32 s2, s2, 0xffff00
	s_add_u32 s2, s4, s2
	s_addc_u32 s3, s5, 0
	global_load_dword v96, v79, s[2:3]
	s_lshl_b32 s2, s25, 8
	s_and_b32 s2, s2, 0xffff00
	s_add_u32 s2, s4, s2
	s_addc_u32 s3, s5, 0
	global_load_dword v94, v79, s[2:3]
	s_lshl_b32 s2, s24, 8
	s_and_b32 s2, s2, 0xffff00
	s_add_u32 s2, s4, s2
	s_addc_u32 s3, s5, 0
	global_load_dword v91, v79, s[2:3]
	s_lshl_b32 s2, s23, 8
	s_and_b32 s2, s2, 0xffff00
	s_add_u32 s2, s4, s2
	s_addc_u32 s3, s5, 0
	global_load_dword v93, v79, s[2:3]
	s_lshl_b32 s2, s42, 8
	s_and_b32 s2, s2, 0xffff00
	s_add_u32 s2, s4, s2
	s_addc_u32 s3, s5, 0
	global_load_dword v90, v79, s[2:3]
	s_lshl_b32 s2, s41, 8
	s_and_b32 s2, s2, 0xffff00
	s_add_u32 s2, s4, s2
	s_addc_u32 s3, s5, 0
	global_load_dword v88, v79, s[2:3]
	s_lshl_b32 s2, s40, 8
	s_and_b32 s2, s2, 0xffff00
	s_add_u32 s2, s4, s2
	s_addc_u32 s3, s5, 0
	global_load_dword v86, v79, s[2:3]
	s_lshl_b32 s2, s39, 8
	s_and_b32 s2, s2, 0xffff00
	s_nop 0
	s_nop 0
	s_add_u32 s2, s4, s2
	s_waitcnt lgkmcnt(0)
	v_mfma_f32_32x32x16_f16 v[32:47], v[16:19], v[82:85], v[32:47]
	v_exp_f32_e32 v0, v0
	v_exp_f32_e32 v1, v1
	s_addc_u32 s3, s5, 0
	global_load_dword v85, v79, s[2:3]
	s_lshl_b32 s2, s38, 8
	s_and_b32 s2, s2, 0xffff00
	s_nop 0
	s_nop 0
	s_add_u32 s2, s4, s2
	v_exp_f32_e32 v6, v6
	v_exp_f32_e32 v7, v7
	s_addc_u32 s3, s5, 0
	global_load_dword v83, v79, s[2:3]
	s_lshl_b32 s2, s37, 8
	s_and_b32 s2, s2, 0xffff00
	s_add_u32 s2, s4, s2
	s_addc_u32 s3, s5, 0
	global_load_dword v92, v79, s[2:3]
	s_lshl_b32 s2, s21, 8
	s_and_b32 s2, s2, 0xffff00
	s_add_u32 s2, s4, s2
	s_addc_u32 s3, s5, 0
	global_load_dword v89, v79, s[2:3]
	s_lshl_b32 s2, s20, 8
	s_and_b32 s2, s2, 0xffff00
	s_add_u32 s2, s4, s2
	s_addc_u32 s3, s5, 0
	s_lshl_b32 s19, s19, 8
	s_and_b32 s19, s19, 0xffff00
	s_add_u32 s20, s4, s19
	s_addc_u32 s21, s5, 0
	s_lshl_b32 s18, s18, 8
	s_and_b32 s18, s18, 0xffff00
	s_add_u32 s18, s4, s18
	s_addc_u32 s19, s5, 0
	s_lshl_b32 s10, s10, 8
	s_and_b32 s10, s10, 0xffff00
	s_add_u32 s24, s4, s10
	s_addc_u32 s25, s5, 0
	global_load_dword v87, v79, s[2:3]
	global_load_dword v84, v79, s[20:21]
	global_load_dword v82, v79, s[18:19]
	global_load_dword v81, v79, s[24:25]
	v_pk_add_f32 v[0:1], v[0:1], 1.0 op_sel_hi:[1,0]
	s_nop 0
	s_nop 0
	v_exp_f32_e32 v16, v4
	v_exp_f32_e32 v17, v5
	v_log_f32_e32 v4, v0
	v_log_f32_e32 v5, v1
	s_nop 0
	s_nop 0
	v_exp_f32_e32 v2, v2
	v_exp_f32_e32 v3, v3
	v_pk_add_f32 v[6:7], v[6:7], 1.0 op_sel_hi:[1,0]
	v_log_f32_e32 v6, v6
	v_log_f32_e32 v7, v7
	v_pk_add_f32 v[0:1], v[16:17], 1.0 op_sel_hi:[1,0]
	v_pk_add_f32 v[2:3], v[2:3], 1.0 op_sel_hi:[1,0]
	v_log_f32_e32 v0, v0
	v_log_f32_e32 v1, v1
	v_exp_f32_e32 v18, v8
	v_exp_f32_e32 v19, v9
	v_log_f32_e32 v8, v2
	v_log_f32_e32 v9, v3
	v_pk_mul_f32 v[2:3], v[48:49], v[6:7] op_sel:[1,0]
	s_nop 0
	s_nop 0
	v_pk_mul_f32 v[0:1], v[48:49], v[0:1] op_sel:[1,0]
	s_nop 0
	s_nop 0
	v_cvt_pk_f16_f32 v3, v2, v3
	v_cvt_pk_f16_f32 v2, v0, v1
	v_pk_mul_f32 v[0:1], v[48:49], v[8:9] op_sel:[1,0]
	v_pk_mul_f32 v[4:5], v[48:49], v[4:5] op_sel:[1,0]
	s_nop 0
	s_nop 0
	s_nop 0
	s_nop 0
	v_cvt_pk_f16_f32 v1, v0, v1
	v_cvt_pk_f16_f32 v0, v4, v5
	v_pk_add_f32 v[4:5], v[18:19], 1.0 op_sel_hi:[1,0]
	v_exp_f32_e32 v6, v10
	v_exp_f32_e32 v7, v11
	v_exp_f32_e32 v8, v12
	v_exp_f32_e32 v9, v13
	v_exp_f32_e32 v10, v14
	v_exp_f32_e32 v11, v15
	v_pk_add_f32 v[8:9], v[8:9], 1.0 op_sel_hi:[1,0]
	v_pk_add_f32 v[10:11], v[10:11], 1.0 op_sel_hi:[1,0]
	v_pk_add_f32 v[6:7], v[6:7], 1.0 op_sel_hi:[1,0]
	v_log_f32_e32 v8, v8
	v_log_f32_e32 v9, v9
	v_log_f32_e32 v10, v10
	v_log_f32_e32 v11, v11
	ds_read_b128 v[12:15], v71
	v_log_f32_e32 v6, v6
	v_log_f32_e32 v7, v7
	v_log_f32_e32 v4, v4
	v_log_f32_e32 v5, v5
	v_pk_mul_f32 v[8:9], v[48:49], v[8:9] op_sel:[1,0]
	v_pk_mul_f32 v[10:11], v[48:49], v[10:11] op_sel:[1,0]
	v_cvt_pk_f16_f32 v118, v8, v9
	v_cvt_pk_f16_f32 v119, v10, v11
	v_pk_mul_f32 v[10:11], v[48:49], v[6:7] op_sel:[1,0]
	ds_read_b128 v[6:9], v71 offset:1024
	s_waitcnt lgkmcnt(1)
	v_mfma_f32_32x32x16_f16 v[16:31], v[0:3], v[12:15], 0
	s_nop 0
	s_nop 0
	v_mul_f32_e64 v4, v49, v4
	v_mul_f32_e64 v5, v49, v5
	v_exp_f32_e32 v32, v32
	v_exp_f32_e32 v33, v33
	s_nop 0
	s_nop 0
	v_cvt_pk_f16_f32 v117, v10, v11
	v_cvt_pk_f16_f32 v116, v4, v5
	v_exp_f32_e32 v36, v36
	v_exp_f32_e32 v37, v37
	v_pk_add_f32 v[32:33], v[32:33], 1.0 op_sel_hi:[1,0]
	s_waitcnt lgkmcnt(0)
	v_mfma_f32_32x32x16_f16 v[16:31], v[116:119], v[6:9], v[16:31]
	v_log_f32_e32 v54, v32
	v_log_f32_e32 v55, v33
	v_pk_add_f32 v[32:33], v[36:37], 1.0 op_sel_hi:[1,0]
	s_nop 0
	s_nop 0
	ds_read_b128 v[4:7], v71 offset:4096
	ds_read_b128 v[120:123], v71 offset:5120
	v_exp_f32_e32 v36, v38
	v_exp_f32_e32 v37, v39
	s_nop 0
	s_nop 0
	s_waitcnt lgkmcnt(1)
	v_mfma_f32_32x32x16_f16 v[0:15], v[0:3], v[4:7], 0
	v_exp_f32_e32 v34, v34
	v_exp_f32_e32 v35, v35
	v_pk_add_f32 v[36:37], v[36:37], 1.0 op_sel_hi:[1,0]
	v_log_f32_e32 v32, v32
	v_log_f32_e32 v33, v33
	v_log_f32_e32 v36, v36
	v_log_f32_e32 v37, v37
	v_pk_add_f32 v[34:35], v[34:35], 1.0 op_sel_hi:[1,0]
	v_pk_mul_f32 v[32:33], v[48:49], v[32:33] op_sel:[1,0]
	v_log_f32_e32 v38, v34
	v_log_f32_e32 v39, v35
	v_pk_mul_f32 v[34:35], v[48:49], v[36:37] op_sel:[1,0]
	v_pk_mul_f32 v[36:37], v[48:49], v[54:55] op_sel:[1,0]
	v_cvt_pk_f16_f32 v35, v34, v35
	v_cvt_pk_f16_f32 v34, v32, v33
	v_pk_mul_f32 v[32:33], v[48:49], v[38:39] op_sel:[1,0]
	s_waitcnt lgkmcnt(0)
	v_mfma_f32_32x32x16_f16 v[0:15], v[116:119], v[120:123], v[0:15]
	v_cvt_pk_f16_f32 v33, v32, v33
	v_cvt_pk_f16_f32 v32, v36, v37
	ds_read_b128 v[36:39], v71 offset:2048
	ds_read_b128 v[116:119], v71 offset:3072
	s_nop 0
	s_nop 0
	v_exp_f32_e32 v55, v44
	v_exp_f32_e32 v115, v45
	s_waitcnt lgkmcnt(1)
	v_mfma_f32_32x32x16_f16 v[16:31], v[32:35], v[36:39], v[16:31]
	ds_read_b128 v[36:39], v71 offset:6144
	v_exp_f32_e32 v44, v40
	v_exp_f32_e32 v45, v41
	v_exp_f32_e32 v52, v42
	v_exp_f32_e32 v54, v43
	ds_read_b128 v[40:43], v71 offset:7168
	s_nop 0
	s_waitcnt lgkmcnt(1)
	v_mfma_f32_32x32x16_f16 v[0:15], v[32:35], v[36:39], v[0:15]
	v_add_f32_e64 v34, v44, 1.0
	v_add_f32_e64 v35, v45, 1.0
	s_nop 0
	s_nop 0
	s_nop 0
	v_log_f32_e32 v36, v34
	v_log_f32_e32 v37, v35
	v_exp_f32_e32 v34, v46
	v_exp_f32_e32 v35, v47
	s_nop 0
	s_nop 0
	v_add_f32_e64 v32, v55, 1.0
	v_add_f32_e64 v33, v115, 1.0
	v_pk_add_f32 v[34:35], v[34:35], 1.0 op_sel_hi:[1,0]
	v_log_f32_e32 v32, v32
	v_log_f32_e32 v33, v33
	v_log_f32_e32 v34, v34
	v_log_f32_e32 v35, v35
	v_add_f32_e64 v38, v52, 1.0
	v_add_f32_e64 v39, v54, 1.0
	v_pk_mul_f32 v[32:33], v[48:49], v[32:33] op_sel:[1,0]
	v_log_f32_e32 v38, v38
	v_log_f32_e32 v39, v39
	v_pk_mul_f32 v[34:35], v[48:49], v[34:35] op_sel:[1,0]
	v_pk_mul_f32 v[36:37], v[48:49], v[36:37] op_sel:[1,0]
	v_cvt_pk_f16_f32 v35, v34, v35
	v_cvt_pk_f16_f32 v34, v32, v33
	v_pk_mul_f32 v[32:33], v[48:49], v[38:39] op_sel:[1,0]
	v_mov_b32_e32 v54, v53
	v_cvt_pk_f16_f32 v33, v32, v33
	v_cvt_pk_f16_f32 v32, v36, v37
	v_cvt_f16_f32_e32 v36, v49
	v_mov_b32_e32 v55, v53
	v_mfma_f32_32x32x16_f16 v[16:31], v[32:35], v[116:119], v[16:31]
	v_cmp_ne_u32_sdwa s[20:21], v95, v50 src0_sel:DWORD src1_sel:WORD_1
	v_cmp_ne_u32_sdwa s[18:19], v99, v50 src0_sel:WORD_1 src1_sel:WORD_1
	s_bitcmp1_b32 s20, 0
	v_cmp_lt_i32_e64 s[2:3], s13, v64
	s_cselect_b64 s[20:21], -1, 0
	s_bitcmp0_b32 s18, 0
	s_waitcnt lgkmcnt(0)
	v_mfma_f32_32x32x16_f16 v[0:15], v[32:35], v[40:43], v[0:15]
	v_cndmask_b32_e64 v32, 0, v36, s[0:1]
	v_pack_b32_f16 v52, v32, 0
	ds_read_b128 v[32:35], v72
	ds_read_b128 v[36:39], v72 offset:1024
	s_nop 0
	s_nop 0
	s_waitcnt lgkmcnt(1)
	v_mfma_f32_32x32x16_f16 v[16:31], v[52:55], v[32:35], v[16:31]
	v_mov_b64_e32 v[32:33], 0
	s_nop 0
	s_waitcnt lgkmcnt(0)
	v_mfma_f32_32x32x16_f16 v[0:15], v[52:55], v[36:39], v[0:15]
	s_nop 11
	v_permlane32_swap_b32_e32 v16, v0
	v_permlane32_swap_b32_e32 v17, v1
	v_permlane32_swap_b32_e32 v18, v2
	v_permlane32_swap_b32_e32 v19, v3
	v_permlane32_swap_b32_e32 v20, v4
	v_permlane32_swap_b32_e32 v21, v5
	v_permlane32_swap_b32_e32 v22, v6
	v_permlane32_swap_b32_e32 v23, v7
	v_permlane32_swap_b32_e32 v24, v8
	v_permlane32_swap_b32_e32 v25, v9
	v_permlane32_swap_b32_e32 v26, v10
	v_permlane32_swap_b32_e32 v27, v11
	v_permlane32_swap_b32_e32 v28, v12
	v_permlane32_swap_b32_e32 v29, v13
	v_permlane32_swap_b32_e32 v30, v14
	v_permlane32_swap_b32_e32 v31, v15
	s_waitcnt vmcnt(31)
	v_fma_mix_f32 v32, v16, v112, v32 op_sel:[0,1,0] op_sel_hi:[0,1,0]
	v_fma_mix_f32 v33, v16, v112, v33 op_sel_hi:[0,1,0]
	s_cbranch_scc1 .LBB4_13
	v_readlane_b32 s10, v50, 0
	s_bfe_u32 s19, s10, 0x80008
	v_lshl_or_b32 v16, s19, 7, v73
	ds_read_u16 v16, v16
	s_bfe_u32 s10, s10, 0x100010
	s_lshl_b32 s10, s10, 8
	s_add_u32 s58, s60, s10
	s_addc_u32 s59, s61, 0
	s_cmp_lg_u64 s[20:21], 0
	s_cselect_b32 s58, s58, s62
	s_cselect_b32 s59, s59, s63
	s_nop 0
	s_waitcnt lgkmcnt(0)
	v_fma_mix_f32 v16, v16, v33, v32 op_sel_hi:[1,0,0]
	s_nop 0
	s_mov_b64 s[20:21], -1
	v_mov_b64_e32 v[32:33], 0
	s_nop 0
	global_store_dword v79, v16, s[58:59] sc1
.LBB4_13:
	s_bitcmp0_b32 s18, 1
	s_waitcnt vmcnt(30)
	v_fma_mix_f32 v32, v17, v110, v32 op_sel:[0,1,0] op_sel_hi:[0,1,0]
	v_fma_mix_f32 v33, v17, v110, v33 op_sel_hi:[0,1,0]
	s_cbranch_scc1 .LBB4_15
	v_readlane_b32 s10, v50, 1
	s_bfe_u32 s19, s10, 0x80008
	v_lshl_or_b32 v16, s19, 7, v73
	ds_read_u16 v34, v16
	s_bfe_u32 s10, s10, 0x100010
	s_lshl_b32 s10, s10, 8
	s_add_u32 s58, s60, s10
	s_addc_u32 s59, s61, 0
	s_cmp_lg_u64 s[20:21], 0
	s_cselect_b32 s58, s58, s62
	s_cselect_b32 s59, s59, s63
	s_nop 0
	s_waitcnt lgkmcnt(0)
	v_fma_mix_f32 v32, v34, v33, v32 op_sel_hi:[1,0,0]
	s_nop 0
	global_store_dword v79, v32, s[58:59] sc1
	s_mov_b64 s[20:21], -1
	v_mov_b64_e32 v[32:33], 0
	s_nop 0
.LBB4_15:
	s_bitcmp0_b32 s18, 2
	s_waitcnt vmcnt(29)
	v_fma_mix_f32 v32, v18, v108, v32 op_sel:[0,1,0] op_sel_hi:[0,1,0]
	v_fma_mix_f32 v33, v18, v108, v33 op_sel_hi:[0,1,0]
	s_cbranch_scc1 .LBB4_17
	v_readlane_b32 s10, v50, 2
	s_bfe_u32 s19, s10, 0x80008
	v_lshl_or_b32 v16, s19, 7, v73
	ds_read_u16 v18, v16
	s_bfe_u32 s10, s10, 0x100010
	s_lshl_b32 s10, s10, 8
	s_add_u32 s58, s60, s10
	s_addc_u32 s59, s61, 0
	s_cmp_lg_u64 s[20:21], 0
	s_cselect_b32 s58, s58, s62
	s_cselect_b32 s59, s59, s63
	s_nop 0
	s_waitcnt lgkmcnt(0)
	v_fma_mix_f32 v18, v18, v33, v32 op_sel_hi:[1,0,0]
	s_nop 0
	s_mov_b64 s[20:21], -1
	v_mov_b64_e32 v[32:33], 0
	s_nop 0
	global_store_dword v79, v18, s[58:59] sc1
.LBB4_17:
	s_bitcmp0_b32 s18, 3
	s_waitcnt vmcnt(28)
	v_fma_mix_f32 v32, v19, v106, v32 op_sel:[0,1,0] op_sel_hi:[0,1,0]
	v_fma_mix_f32 v33, v19, v106, v33 op_sel_hi:[0,1,0]
	s_cbranch_scc1 .LBB4_19
	v_readlane_b32 s10, v50, 3
	s_bfe_u32 s19, s10, 0x80008
	v_lshl_or_b32 v16, s19, 7, v73
	ds_read_u16 v18, v16
	s_bfe_u32 s10, s10, 0x100010
	s_lshl_b32 s10, s10, 8
	s_add_u32 s58, s60, s10
	s_addc_u32 s59, s61, 0
	s_cmp_lg_u64 s[20:21], 0
	s_cselect_b32 s58, s58, s62
	s_cselect_b32 s59, s59, s63
	s_nop 0
	s_waitcnt lgkmcnt(0)
	v_fma_mix_f32 v18, v18, v33, v32 op_sel_hi:[1,0,0]
	s_nop 0
	s_mov_b64 s[20:21], -1
	v_mov_b64_e32 v[32:33], 0
	s_nop 0
	global_store_dword v79, v18, s[58:59] sc1
.LBB4_19:
	s_bitcmp0_b32 s18, 4
	s_waitcnt vmcnt(27)
	v_fma_mix_f32 v32, v0, v104, v32 op_sel:[0,1,0] op_sel_hi:[0,1,0]
	v_fma_mix_f32 v33, v0, v104, v33 op_sel_hi:[0,1,0]
	s_cbranch_scc1 .LBB4_21
	v_readlane_b32 s10, v50, 4
	s_bfe_u32 s19, s10, 0x80008
	v_lshl_or_b32 v0, s19, 7, v73
	ds_read_u16 v0, v0
	s_bfe_u32 s10, s10, 0x100010
	s_lshl_b32 s10, s10, 8
	s_add_u32 s58, s60, s10
	s_addc_u32 s59, s61, 0
	s_cmp_lg_u64 s[20:21], 0
	s_cselect_b32 s58, s58, s62
	s_cselect_b32 s59, s59, s63
	s_nop 0
	s_waitcnt lgkmcnt(0)
	v_fma_mix_f32 v0, v0, v33, v32 op_sel_hi:[1,0,0]
	s_nop 0
	s_mov_b64 s[20:21], -1
	v_mov_b64_e32 v[32:33], 0
	s_nop 0
	global_store_dword v79, v0, s[58:59] sc1
.LBB4_21:
	s_bitcmp0_b32 s18, 5
	s_waitcnt vmcnt(26)
	v_fma_mix_f32 v32, v1, v102, v32 op_sel:[0,1,0] op_sel_hi:[0,1,0]
	v_fma_mix_f32 v33, v1, v102, v33 op_sel_hi:[0,1,0]
	s_cbranch_scc1 .LBB4_23
	v_readlane_b32 s10, v50, 5
	s_bfe_u32 s19, s10, 0x80008
	v_lshl_or_b32 v0, s19, 7, v73
	ds_read_u16 v16, v0
	s_bfe_u32 s10, s10, 0x100010
	s_lshl_b32 s10, s10, 8
	s_add_u32 s58, s60, s10
	s_addc_u32 s59, s61, 0
	s_cmp_lg_u64 s[20:21], 0
	s_cselect_b32 s58, s58, s62
	s_cselect_b32 s59, s59, s63
	s_nop 0
	s_waitcnt lgkmcnt(0)
	v_fma_mix_f32 v16, v16, v33, v32 op_sel_hi:[1,0,0]
	s_nop 0
	s_mov_b64 s[20:21], -1
	v_mov_b64_e32 v[32:33], 0
	s_nop 0
	global_store_dword v79, v16, s[58:59] sc1
.LBB4_23:
	s_bitcmp0_b32 s18, 6
	s_waitcnt vmcnt(25)
	v_fma_mix_f32 v32, v2, v100, v32 op_sel:[0,1,0] op_sel_hi:[0,1,0]
	v_fma_mix_f32 v33, v2, v100, v33 op_sel_hi:[0,1,0]
	s_cbranch_scc1 .LBB4_25
	v_readlane_b32 s10, v50, 6
	s_bfe_u32 s19, s10, 0x80008
	v_lshl_or_b32 v0, s19, 7, v73
	ds_read_u16 v2, v0
	s_bfe_u32 s10, s10, 0x100010
	s_lshl_b32 s10, s10, 8
	s_add_u32 s58, s60, s10
	s_addc_u32 s59, s61, 0
	s_cmp_lg_u64 s[20:21], 0
	s_cselect_b32 s58, s58, s62
	s_cselect_b32 s59, s59, s63
	s_nop 0
	s_waitcnt lgkmcnt(0)
	v_fma_mix_f32 v2, v2, v33, v32 op_sel_hi:[1,0,0]
	s_nop 0
	s_mov_b64 s[20:21], -1
	v_mov_b64_e32 v[32:33], 0
	s_nop 0
	global_store_dword v79, v2, s[58:59] sc1
.LBB4_25:
	s_bitcmp0_b32 s18, 7
	s_waitcnt vmcnt(24)
	v_fma_mix_f32 v32, v3, v114, v32 op_sel:[0,1,0] op_sel_hi:[0,1,0]
	v_fma_mix_f32 v33, v3, v114, v33 op_sel_hi:[0,1,0]
	s_cbranch_scc1 .LBB4_27
	v_readlane_b32 s10, v50, 7
	s_bfe_u32 s19, s10, 0x80008
	v_lshl_or_b32 v0, s19, 7, v73
	ds_read_u16 v2, v0
	s_bfe_u32 s10, s10, 0x100010
	s_lshl_b32 s10, s10, 8
	s_add_u32 s58, s60, s10
	s_addc_u32 s59, s61, 0
	s_cmp_lg_u64 s[20:21], 0
	s_cselect_b32 s58, s58, s62
	s_cselect_b32 s59, s59, s63
	s_nop 0
	s_waitcnt lgkmcnt(0)
	v_fma_mix_f32 v2, v2, v33, v32 op_sel_hi:[1,0,0]
	s_nop 0
	s_mov_b64 s[20:21], -1
	v_mov_b64_e32 v[32:33], 0
	s_nop 0
	global_store_dword v79, v2, s[58:59] sc1
.LBB4_27:
	s_bitcmp0_b32 s18, 8
	s_waitcnt vmcnt(23)
	v_fma_mix_f32 v32, v20, v113, v32 op_sel:[0,1,0] op_sel_hi:[0,1,0]
	v_fma_mix_f32 v33, v20, v113, v33 op_sel_hi:[0,1,0]
	s_cbranch_scc1 .LBB4_29
	v_readlane_b32 s10, v50, 8
	s_bfe_u32 s19, s10, 0x80008
	v_lshl_or_b32 v0, s19, 7, v73
	ds_read_u16 v2, v0
	s_bfe_u32 s10, s10, 0x100010
	s_lshl_b32 s10, s10, 8
	s_add_u32 s58, s60, s10
	s_addc_u32 s59, s61, 0
	s_cmp_lg_u64 s[20:21], 0
	s_cselect_b32 s58, s58, s62
	s_cselect_b32 s59, s59, s63
	s_nop 0
	s_waitcnt lgkmcnt(0)
	v_fma_mix_f32 v2, v2, v33, v32 op_sel_hi:[1,0,0]
	s_nop 0
	s_mov_b64 s[20:21], -1
	v_mov_b64_e32 v[32:33], 0
	s_nop 0
	global_store_dword v79, v2, s[58:59] sc1
.LBB4_29:
	s_bitcmp0_b32 s18, 9
	s_waitcnt vmcnt(22)
	v_fma_mix_f32 v32, v21, v111, v32 op_sel:[0,1,0] op_sel_hi:[0,1,0]
	v_fma_mix_f32 v33, v21, v111, v33 op_sel_hi:[0,1,0]
	s_cbranch_scc1 .LBB4_31
	v_readlane_b32 s10, v50, 9
	s_bfe_u32 s19, s10, 0x80008
	v_lshl_or_b32 v0, s19, 7, v73
	ds_read_u16 v2, v0
	s_bfe_u32 s10, s10, 0x100010
	s_lshl_b32 s10, s10, 8
	s_add_u32 s58, s60, s10
	s_addc_u32 s59, s61, 0
	s_cmp_lg_u64 s[20:21], 0
	s_cselect_b32 s58, s58, s62
	s_cselect_b32 s59, s59, s63
	s_nop 0
	s_waitcnt lgkmcnt(0)
	v_fma_mix_f32 v2, v2, v33, v32 op_sel_hi:[1,0,0]
	s_nop 0
	s_mov_b64 s[20:21], -1
	v_mov_b64_e32 v[32:33], 0
	s_nop 0
	global_store_dword v79, v2, s[58:59] sc1
.LBB4_31:
	s_bitcmp0_b32 s18, 10
	s_waitcnt vmcnt(21)
	v_fma_mix_f32 v32, v22, v109, v32 op_sel:[0,1,0] op_sel_hi:[0,1,0]
	v_fma_mix_f32 v33, v22, v109, v33 op_sel_hi:[0,1,0]
	s_cbranch_scc1 .LBB4_33
	v_readlane_b32 s10, v50, 10
	s_bfe_u32 s19, s10, 0x80008
	v_lshl_or_b32 v0, s19, 7, v73
	ds_read_u16 v2, v0
	s_bfe_u32 s10, s10, 0x100010
	s_lshl_b32 s10, s10, 8
	s_add_u32 s58, s60, s10
	s_addc_u32 s59, s61, 0
	s_cmp_lg_u64 s[20:21], 0
	s_cselect_b32 s58, s58, s62
	s_cselect_b32 s59, s59, s63
	s_nop 0
	s_waitcnt lgkmcnt(0)
	v_fma_mix_f32 v2, v2, v33, v32 op_sel_hi:[1,0,0]
	s_nop 0
	s_mov_b64 s[20:21], -1
	v_mov_b64_e32 v[32:33], 0
	s_nop 0
	global_store_dword v79, v2, s[58:59] sc1
.LBB4_33:
	s_bitcmp0_b32 s18, 11
	s_waitcnt vmcnt(20)
	v_fma_mix_f32 v32, v23, v107, v32 op_sel:[0,1,0] op_sel_hi:[0,1,0]
	v_fma_mix_f32 v33, v23, v107, v33 op_sel_hi:[0,1,0]
	s_cbranch_scc1 .LBB4_35
	v_readlane_b32 s10, v50, 11
	s_bfe_u32 s19, s10, 0x80008
	v_lshl_or_b32 v0, s19, 7, v73
	ds_read_u16 v2, v0
	s_bfe_u32 s10, s10, 0x100010
	s_lshl_b32 s10, s10, 8
	s_add_u32 s58, s60, s10
	s_addc_u32 s59, s61, 0
	s_cmp_lg_u64 s[20:21], 0
	s_cselect_b32 s58, s58, s62
	s_cselect_b32 s59, s59, s63
	s_nop 0
	s_waitcnt lgkmcnt(0)
	v_fma_mix_f32 v2, v2, v33, v32 op_sel_hi:[1,0,0]
	s_nop 0
	s_mov_b64 s[20:21], -1
	v_mov_b64_e32 v[32:33], 0
	s_nop 0
	global_store_dword v79, v2, s[58:59] sc1
.LBB4_35:
	s_bitcmp0_b32 s18, 12
	s_waitcnt vmcnt(19)
	v_fma_mix_f32 v32, v4, v105, v32 op_sel:[0,1,0] op_sel_hi:[0,1,0]
	v_fma_mix_f32 v33, v4, v105, v33 op_sel_hi:[0,1,0]
	s_cbranch_scc1 .LBB4_37
	v_readlane_b32 s10, v50, 12
	s_bfe_u32 s19, s10, 0x80008
	v_lshl_or_b32 v0, s19, 7, v73
	ds_read_u16 v2, v0
	s_bfe_u32 s10, s10, 0x100010
	s_lshl_b32 s10, s10, 8
	s_add_u32 s58, s60, s10
	s_addc_u32 s59, s61, 0
	s_cmp_lg_u64 s[20:21], 0
	s_cselect_b32 s58, s58, s62
	s_cselect_b32 s59, s59, s63
	s_nop 0
	s_waitcnt lgkmcnt(0)
	v_fma_mix_f32 v2, v2, v33, v32 op_sel_hi:[1,0,0]
	s_nop 0
	s_mov_b64 s[20:21], -1
	v_mov_b64_e32 v[32:33], 0
	s_nop 0
	global_store_dword v79, v2, s[58:59] sc1
.LBB4_37:
	s_bitcmp0_b32 s18, 13
	s_waitcnt vmcnt(18)
	v_fma_mix_f32 v32, v5, v103, v32 op_sel:[0,1,0] op_sel_hi:[0,1,0]
	v_fma_mix_f32 v33, v5, v103, v33 op_sel_hi:[0,1,0]
	s_cbranch_scc1 .LBB4_39
	v_readlane_b32 s10, v50, 13
	s_bfe_u32 s19, s10, 0x80008
	v_lshl_or_b32 v0, s19, 7, v73
	ds_read_u16 v2, v0
	s_bfe_u32 s10, s10, 0x100010
	s_lshl_b32 s10, s10, 8
	s_add_u32 s58, s60, s10
	s_addc_u32 s59, s61, 0
	s_cmp_lg_u64 s[20:21], 0
	s_cselect_b32 s58, s58, s62
	s_cselect_b32 s59, s59, s63
	s_nop 0
	s_waitcnt lgkmcnt(0)
	v_fma_mix_f32 v2, v2, v33, v32 op_sel_hi:[1,0,0]
	s_nop 0
	s_mov_b64 s[20:21], -1
	v_mov_b64_e32 v[32:33], 0
	s_nop 0
	global_store_dword v79, v2, s[58:59] sc1
.LBB4_39:
	s_bitcmp0_b32 s18, 14
	s_waitcnt vmcnt(17)
	v_fma_mix_f32 v32, v6, v101, v32 op_sel:[0,1,0] op_sel_hi:[0,1,0]
	v_fma_mix_f32 v33, v6, v101, v33 op_sel_hi:[0,1,0]
	s_cbranch_scc1 .LBB4_41
	v_readlane_b32 s10, v50, 14
	s_bfe_u32 s19, s10, 0x80008
	v_lshl_or_b32 v0, s19, 7, v73
	ds_read_u16 v2, v0
	s_bfe_u32 s10, s10, 0x100010
	s_lshl_b32 s10, s10, 8
	s_add_u32 s58, s60, s10
	s_addc_u32 s59, s61, 0
	s_cmp_lg_u64 s[20:21], 0
	s_cselect_b32 s58, s58, s62
	s_cselect_b32 s59, s59, s63
	s_nop 0
	s_waitcnt lgkmcnt(0)
	v_fma_mix_f32 v2, v2, v33, v32 op_sel_hi:[1,0,0]
	s_nop 0
	s_mov_b64 s[20:21], -1
	v_mov_b64_e32 v[32:33], 0
	s_nop 0
	global_store_dword v79, v2, s[58:59] sc1
.LBB4_41:
	s_bitcmp0_b32 s18, 15
	s_waitcnt vmcnt(16)
	v_fma_mix_f32 v32, v7, v98, v32 op_sel:[0,1,0] op_sel_hi:[0,1,0]
	v_fma_mix_f32 v33, v7, v98, v33 op_sel_hi:[0,1,0]
	s_cbranch_scc1 .LBB4_43
	v_readlane_b32 s10, v50, 15
	s_bfe_u32 s19, s10, 0x80008
	v_lshl_or_b32 v0, s19, 7, v73
	ds_read_u16 v2, v0
	s_bfe_u32 s10, s10, 0x100010
	s_lshl_b32 s10, s10, 8
	s_add_u32 s58, s60, s10
	s_addc_u32 s59, s61, 0
	s_cmp_lg_u64 s[20:21], 0
	s_cselect_b32 s58, s58, s62
	s_cselect_b32 s59, s59, s63
	s_nop 0
	s_waitcnt lgkmcnt(0)
	v_fma_mix_f32 v2, v2, v33, v32 op_sel_hi:[1,0,0]
	s_nop 0
	s_mov_b64 s[20:21], -1
	v_mov_b64_e32 v[32:33], 0
	s_nop 0
	global_store_dword v79, v2, s[58:59] sc1
.LBB4_43:
	s_bitcmp0_b32 s18, 16
	s_waitcnt vmcnt(15)
	v_fma_mix_f32 v32, v24, v97, v32 op_sel:[0,1,0] op_sel_hi:[0,1,0]
	v_fma_mix_f32 v33, v24, v97, v33 op_sel_hi:[0,1,0]
	s_cbranch_scc1 .LBB4_45
	v_readlane_b32 s10, v50, 16
	s_bfe_u32 s19, s10, 0x80008
	v_lshl_or_b32 v0, s19, 7, v73
	ds_read_u16 v2, v0
	s_bfe_u32 s10, s10, 0x100010
	s_lshl_b32 s10, s10, 8
	s_add_u32 s58, s60, s10
	s_addc_u32 s59, s61, 0
	s_cmp_lg_u64 s[20:21], 0
	s_cselect_b32 s58, s58, s62
	s_cselect_b32 s59, s59, s63
	s_nop 0
	s_waitcnt lgkmcnt(0)
	v_fma_mix_f32 v2, v2, v33, v32 op_sel_hi:[1,0,0]
	s_nop 0
	s_mov_b64 s[20:21], -1
	v_mov_b64_e32 v[32:33], 0
	s_nop 0
	global_store_dword v79, v2, s[58:59] sc1
.LBB4_45:
	s_bitcmp0_b32 s18, 17
	s_waitcnt vmcnt(14)
	v_fma_mix_f32 v32, v25, v96, v32 op_sel:[0,1,0] op_sel_hi:[0,1,0]
	v_fma_mix_f32 v33, v25, v96, v33 op_sel_hi:[0,1,0]
	s_cbranch_scc1 .LBB4_47
	v_readlane_b32 s10, v50, 17
	s_bfe_u32 s19, s10, 0x80008
	v_lshl_or_b32 v0, s19, 7, v73
	ds_read_u16 v2, v0
	s_bfe_u32 s10, s10, 0x100010
	s_lshl_b32 s10, s10, 8
	s_add_u32 s58, s60, s10
	s_addc_u32 s59, s61, 0
	s_cmp_lg_u64 s[20:21], 0
	s_cselect_b32 s58, s58, s62
	s_cselect_b32 s59, s59, s63
	s_nop 0
	s_waitcnt lgkmcnt(0)
	v_fma_mix_f32 v2, v2, v33, v32 op_sel_hi:[1,0,0]
	s_nop 0
	s_mov_b64 s[20:21], -1
	v_mov_b64_e32 v[32:33], 0
	s_nop 0
	global_store_dword v79, v2, s[58:59] sc1
.LBB4_47:
	s_bitcmp0_b32 s18, 18
	s_waitcnt vmcnt(13)
	v_fma_mix_f32 v32, v26, v94, v32 op_sel:[0,1,0] op_sel_hi:[0,1,0]
	v_fma_mix_f32 v33, v26, v94, v33 op_sel_hi:[0,1,0]
	s_cbranch_scc1 .LBB4_49
	v_readlane_b32 s10, v50, 18
	s_bfe_u32 s19, s10, 0x80008
	v_lshl_or_b32 v0, s19, 7, v73
	ds_read_u16 v2, v0
	s_bfe_u32 s10, s10, 0x100010
	s_lshl_b32 s10, s10, 8
	s_add_u32 s58, s60, s10
	s_addc_u32 s59, s61, 0
	s_cmp_lg_u64 s[20:21], 0
	s_cselect_b32 s58, s58, s62
	s_cselect_b32 s59, s59, s63
	s_nop 0
	s_waitcnt lgkmcnt(0)
	v_fma_mix_f32 v2, v2, v33, v32 op_sel_hi:[1,0,0]
	s_nop 0
	s_mov_b64 s[20:21], -1
	v_mov_b64_e32 v[32:33], 0
	s_nop 0
	global_store_dword v79, v2, s[58:59] sc1
.LBB4_49:
	s_bitcmp0_b32 s18, 19
	s_waitcnt vmcnt(12)
	v_fma_mix_f32 v32, v27, v91, v32 op_sel:[0,1,0] op_sel_hi:[0,1,0]
	v_fma_mix_f32 v33, v27, v91, v33 op_sel_hi:[0,1,0]
	s_cbranch_scc1 .LBB4_51
	v_readlane_b32 s10, v50, 19
	s_bfe_u32 s19, s10, 0x80008
	v_lshl_or_b32 v0, s19, 7, v73
	ds_read_u16 v2, v0
	s_bfe_u32 s10, s10, 0x100010
	s_lshl_b32 s10, s10, 8
	s_add_u32 s58, s60, s10
	s_addc_u32 s59, s61, 0
	s_cmp_lg_u64 s[20:21], 0
	s_cselect_b32 s58, s58, s62
	s_cselect_b32 s59, s59, s63
	s_nop 0
	s_waitcnt lgkmcnt(0)
	v_fma_mix_f32 v2, v2, v33, v32 op_sel_hi:[1,0,0]
	s_nop 0
	s_mov_b64 s[20:21], -1
	v_mov_b64_e32 v[32:33], 0
	s_nop 0
	global_store_dword v79, v2, s[58:59] sc1
.LBB4_51:
	s_bitcmp0_b32 s18, 20
	s_waitcnt vmcnt(11)
	v_fma_mix_f32 v32, v8, v93, v32 op_sel:[0,1,0] op_sel_hi:[0,1,0]
	v_fma_mix_f32 v33, v8, v93, v33 op_sel_hi:[0,1,0]
	s_cbranch_scc1 .LBB4_53
	v_readlane_b32 s10, v50, 20
	s_bfe_u32 s19, s10, 0x80008
	v_lshl_or_b32 v0, s19, 7, v73
	ds_read_u16 v2, v0
	s_bfe_u32 s10, s10, 0x100010
	s_lshl_b32 s10, s10, 8
	s_add_u32 s58, s60, s10
	s_addc_u32 s59, s61, 0
	s_cmp_lg_u64 s[20:21], 0
	s_cselect_b32 s58, s58, s62
	s_cselect_b32 s59, s59, s63
	s_nop 0
	s_waitcnt lgkmcnt(0)
	v_fma_mix_f32 v2, v2, v33, v32 op_sel_hi:[1,0,0]
	s_nop 0
	s_mov_b64 s[20:21], -1
	v_mov_b64_e32 v[32:33], 0
	s_nop 0
	global_store_dword v79, v2, s[58:59] sc1
.LBB4_53:
	s_bitcmp0_b32 s18, 21
	s_waitcnt vmcnt(10)
	v_fma_mix_f32 v32, v9, v90, v32 op_sel:[0,1,0] op_sel_hi:[0,1,0]
	v_fma_mix_f32 v33, v9, v90, v33 op_sel_hi:[0,1,0]
	s_cbranch_scc1 .LBB4_55
	v_readlane_b32 s10, v50, 21
	s_bfe_u32 s19, s10, 0x80008
	v_lshl_or_b32 v0, s19, 7, v73
	ds_read_u16 v2, v0
	s_bfe_u32 s10, s10, 0x100010
	s_lshl_b32 s10, s10, 8
	s_add_u32 s58, s60, s10
	s_addc_u32 s59, s61, 0
	s_cmp_lg_u64 s[20:21], 0
	s_cselect_b32 s58, s58, s62
	s_cselect_b32 s59, s59, s63
	s_nop 0
	s_waitcnt lgkmcnt(0)
	v_fma_mix_f32 v2, v2, v33, v32 op_sel_hi:[1,0,0]
	s_nop 0
	s_mov_b64 s[20:21], -1
	v_mov_b64_e32 v[32:33], 0
	s_nop 0
	global_store_dword v79, v2, s[58:59] sc1
.LBB4_55:
	s_bitcmp0_b32 s18, 22
	s_waitcnt vmcnt(9)
	v_fma_mix_f32 v32, v10, v88, v32 op_sel:[0,1,0] op_sel_hi:[0,1,0]
	v_fma_mix_f32 v33, v10, v88, v33 op_sel_hi:[0,1,0]
	s_cbranch_scc1 .LBB4_57
	v_readlane_b32 s10, v50, 22
	s_bfe_u32 s19, s10, 0x80008
	v_lshl_or_b32 v0, s19, 7, v73
	ds_read_u16 v2, v0
	s_bfe_u32 s10, s10, 0x100010
	s_lshl_b32 s10, s10, 8
	s_add_u32 s58, s60, s10
	s_addc_u32 s59, s61, 0
	s_cmp_lg_u64 s[20:21], 0
	s_cselect_b32 s58, s58, s62
	s_cselect_b32 s59, s59, s63
	s_nop 0
	s_waitcnt lgkmcnt(0)
	v_fma_mix_f32 v2, v2, v33, v32 op_sel_hi:[1,0,0]
	s_nop 0
	s_mov_b64 s[20:21], -1
	v_mov_b64_e32 v[32:33], 0
	s_nop 0
	global_store_dword v79, v2, s[58:59] sc1
.LBB4_57:
	s_bitcmp0_b32 s18, 23
	s_waitcnt vmcnt(8)
	v_fma_mix_f32 v32, v11, v86, v32 op_sel:[0,1,0] op_sel_hi:[0,1,0]
	v_fma_mix_f32 v33, v11, v86, v33 op_sel_hi:[0,1,0]
	s_cbranch_scc1 .LBB4_59
	v_readlane_b32 s10, v50, 23
	s_bfe_u32 s19, s10, 0x80008
	v_lshl_or_b32 v0, s19, 7, v73
	ds_read_u16 v2, v0
	s_bfe_u32 s10, s10, 0x100010
	s_lshl_b32 s10, s10, 8
	s_add_u32 s58, s60, s10
	s_addc_u32 s59, s61, 0
	s_cmp_lg_u64 s[20:21], 0
	s_cselect_b32 s58, s58, s62
	s_cselect_b32 s59, s59, s63
	s_nop 0
	s_waitcnt lgkmcnt(0)
	v_fma_mix_f32 v2, v2, v33, v32 op_sel_hi:[1,0,0]
	s_nop 0
	s_mov_b64 s[20:21], -1
	v_mov_b64_e32 v[32:33], 0
	s_nop 0
	global_store_dword v79, v2, s[58:59] sc1
.LBB4_59:
	s_bitcmp0_b32 s18, 24
	s_waitcnt vmcnt(7)
	v_fma_mix_f32 v32, v28, v85, v32 op_sel:[0,1,0] op_sel_hi:[0,1,0]
	v_fma_mix_f32 v33, v28, v85, v33 op_sel_hi:[0,1,0]
	s_cbranch_scc1 .LBB4_61
	v_readlane_b32 s10, v50, 24
	s_bfe_u32 s19, s10, 0x80008
	v_lshl_or_b32 v0, s19, 7, v73
	ds_read_u16 v2, v0
	s_bfe_u32 s10, s10, 0x100010
	s_lshl_b32 s10, s10, 8
	s_add_u32 s58, s60, s10
	s_addc_u32 s59, s61, 0
	s_cmp_lg_u64 s[20:21], 0
	s_cselect_b32 s58, s58, s62
	s_cselect_b32 s59, s59, s63
	s_nop 0
	s_waitcnt lgkmcnt(0)
	v_fma_mix_f32 v2, v2, v33, v32 op_sel_hi:[1,0,0]
	s_nop 0
	s_mov_b64 s[20:21], -1
	v_mov_b64_e32 v[32:33], 0
	s_nop 0
	global_store_dword v79, v2, s[58:59] sc1
.LBB4_61:
	s_bitcmp0_b32 s18, 25
	s_waitcnt vmcnt(6)
	v_fma_mix_f32 v32, v29, v83, v32 op_sel:[0,1,0] op_sel_hi:[0,1,0]
	v_fma_mix_f32 v33, v29, v83, v33 op_sel_hi:[0,1,0]
	s_cbranch_scc1 .LBB4_63
	v_readlane_b32 s10, v50, 25
	s_bfe_u32 s19, s10, 0x80008
	v_lshl_or_b32 v0, s19, 7, v73
	ds_read_u16 v2, v0
	s_bfe_u32 s10, s10, 0x100010
	s_lshl_b32 s10, s10, 8
	s_add_u32 s58, s60, s10
	s_addc_u32 s59, s61, 0
	s_cmp_lg_u64 s[20:21], 0
	s_cselect_b32 s58, s58, s62
	s_cselect_b32 s59, s59, s63
	s_nop 0
	s_waitcnt lgkmcnt(0)
	v_fma_mix_f32 v2, v2, v33, v32 op_sel_hi:[1,0,0]
	s_nop 0
	s_mov_b64 s[20:21], -1
	v_mov_b64_e32 v[32:33], 0
	s_nop 0
	global_store_dword v79, v2, s[58:59] sc1
.LBB4_63:
	s_bitcmp0_b32 s18, 26
	s_waitcnt vmcnt(5)
	v_fma_mix_f32 v32, v30, v92, v32 op_sel:[0,1,0] op_sel_hi:[0,1,0]
	v_fma_mix_f32 v33, v30, v92, v33 op_sel_hi:[0,1,0]
	s_cbranch_scc1 .LBB4_65
	v_readlane_b32 s10, v50, 26
	s_bfe_u32 s19, s10, 0x80008
	v_lshl_or_b32 v0, s19, 7, v73
	ds_read_u16 v2, v0
	s_bfe_u32 s10, s10, 0x100010
	s_lshl_b32 s10, s10, 8
	s_add_u32 s58, s60, s10
	s_addc_u32 s59, s61, 0
	s_cmp_lg_u64 s[20:21], 0
	s_cselect_b32 s58, s58, s62
	s_cselect_b32 s59, s59, s63
	s_nop 0
	s_waitcnt lgkmcnt(0)
	v_fma_mix_f32 v2, v2, v33, v32 op_sel_hi:[1,0,0]
	s_nop 0
	s_mov_b64 s[20:21], -1
	v_mov_b64_e32 v[32:33], 0
	s_nop 0
	global_store_dword v79, v2, s[58:59] sc1
.LBB4_65:
	s_bitcmp0_b32 s18, 27
	s_waitcnt vmcnt(4)
	v_fma_mix_f32 v32, v31, v89, v32 op_sel:[0,1,0] op_sel_hi:[0,1,0]
	v_fma_mix_f32 v33, v31, v89, v33 op_sel_hi:[0,1,0]
	s_cbranch_scc1 .LBB4_67
	v_readlane_b32 s10, v50, 27
	s_bfe_u32 s19, s10, 0x80008
	v_lshl_or_b32 v0, s19, 7, v73
	ds_read_u16 v2, v0
	s_bfe_u32 s10, s10, 0x100010
	s_lshl_b32 s10, s10, 8
	s_add_u32 s58, s60, s10
	s_addc_u32 s59, s61, 0
	s_cmp_lg_u64 s[20:21], 0
	s_cselect_b32 s58, s58, s62
	s_cselect_b32 s59, s59, s63
	s_nop 0
	s_waitcnt lgkmcnt(0)
	v_fma_mix_f32 v2, v2, v33, v32 op_sel_hi:[1,0,0]
	s_nop 0
	s_mov_b64 s[20:21], -1
	v_mov_b64_e32 v[32:33], 0
	s_nop 0
	global_store_dword v79, v2, s[58:59] sc1
.LBB4_67:
	s_bitcmp0_b32 s18, 28
	s_waitcnt vmcnt(3)
	v_fma_mix_f32 v32, v12, v87, v32 op_sel:[0,1,0] op_sel_hi:[0,1,0]
	v_fma_mix_f32 v33, v12, v87, v33 op_sel_hi:[0,1,0]
	s_cbranch_scc1 .LBB4_69
	v_readlane_b32 s10, v50, 28
	s_bfe_u32 s19, s10, 0x80008
	v_lshl_or_b32 v0, s19, 7, v73
	ds_read_u16 v2, v0
	s_bfe_u32 s10, s10, 0x100010
	s_lshl_b32 s10, s10, 8
	s_add_u32 s58, s60, s10
	s_addc_u32 s59, s61, 0
	s_cmp_lg_u64 s[20:21], 0
	s_cselect_b32 s58, s58, s62
	s_cselect_b32 s59, s59, s63
	s_nop 0
	s_waitcnt lgkmcnt(0)
	v_fma_mix_f32 v2, v2, v33, v32 op_sel_hi:[1,0,0]
	s_nop 0
	s_mov_b64 s[20:21], -1
	v_mov_b64_e32 v[32:33], 0
	s_nop 0
	global_store_dword v79, v2, s[58:59] sc1
.LBB4_69:
	s_bitcmp0_b32 s18, 29
	s_waitcnt vmcnt(2)
	v_fma_mix_f32 v32, v13, v84, v32 op_sel:[0,1,0] op_sel_hi:[0,1,0]
	v_fma_mix_f32 v33, v13, v84, v33 op_sel_hi:[0,1,0]
	s_cbranch_scc1 .LBB4_71
	v_readlane_b32 s10, v50, 29
	s_bfe_u32 s19, s10, 0x80008
	v_lshl_or_b32 v0, s19, 7, v73
	ds_read_u16 v2, v0
	s_bfe_u32 s10, s10, 0x100010
	s_lshl_b32 s10, s10, 8
	s_add_u32 s58, s60, s10
	s_addc_u32 s59, s61, 0
	s_cmp_lg_u64 s[20:21], 0
	s_cselect_b32 s58, s58, s62
	s_cselect_b32 s59, s59, s63
	s_nop 0
	s_waitcnt lgkmcnt(0)
	v_fma_mix_f32 v2, v2, v33, v32 op_sel_hi:[1,0,0]
	s_nop 0
	s_mov_b64 s[20:21], -1
	v_mov_b64_e32 v[32:33], 0
	s_nop 0
	global_store_dword v79, v2, s[58:59] sc1
.LBB4_71:
	s_bitcmp0_b32 s18, 30
	s_waitcnt vmcnt(1)
	v_fma_mix_f32 v32, v14, v82, v32 op_sel:[0,1,0] op_sel_hi:[0,1,0]
	v_fma_mix_f32 v33, v14, v82, v33 op_sel_hi:[0,1,0]
	s_cbranch_scc1 .LBB4_10
	v_readlane_b32 s10, v50, 30
	s_bfe_u32 s18, s10, 0x80008
	v_lshl_or_b32 v0, s18, 7, v73
	ds_read_u16 v2, v0
	s_bfe_u32 s10, s10, 0x100010
	s_lshl_b32 s10, s10, 8
	s_add_u32 s58, s60, s10
	s_addc_u32 s59, s61, 0
	s_cmp_lg_u64 s[20:21], 0
	s_cselect_b32 s58, s58, s62
	s_cselect_b32 s59, s59, s63
	s_nop 0
	s_waitcnt lgkmcnt(0)
	v_fma_mix_f32 v2, v2, v33, v32 op_sel_hi:[1,0,0]
	s_nop 0
	s_mov_b64 s[20:21], -1
	v_mov_b64_e32 v[32:33], 0
	s_nop 0
	global_store_dword v79, v2, s[58:59] sc1
	s_branch .LBB4_10
